# attention type-A tile loops: waves 4-7 take their per-tile barrier between softmax and PV (half-tile stagger), V^T tiles triple-buffered in LDS
# speedup vs baseline: 1.0061x; 1.0061x over previous
.LBB6_1252:
	s_and_b64 vcc, exec, s[6:7]
	s_cbranch_vccz .LBB6_1288
	s_lshl_b32 s48, s37, 8
	s_lshl_b32 s0, s36, 11
	v_readlane_b32 s28, v254, 13
	s_add_i32 s1, s48, 0x100
	s_add_i32 s34, s48, s0
	s_mov_b32 s35, s85
	v_readlane_b32 s29, v254, 14
	s_lshr_b32 s47, s1, 6
	s_lshl_b64 s[0:1], s[34:35], 10
	s_add_u32 s0, s28, s0
	s_addc_u32 s1, s29, s1
	s_lshl_b32 s30, s74, 1
	s_add_u32 s0, s0, s30
	s_addc_u32 s1, s1, 0
	s_add_u32 s24, s0, 0x6200000
	s_addc_u32 s25, s1, 0
	s_lshl_b32 s0, s36, 21
	s_add_u32 s0, s28, s0
	s_addc_u32 s1, s29, 0
	s_add_u32 s0, s0, s30
	s_addc_u32 s1, s1, 0
	s_add_u32 s26, s0, 0x6a00000
	v_mov_b32_e32 v145, v0
	s_addc_u32 s27, s1, 0
	s_waitcnt vmcnt(0)
	v_mov_b32_e32 v22, v0
	s_add_u32 s0, s28, s75
	s_addc_u32 s1, s29, 0
	v_ashrrev_i32_e32 v2, 31, v22
	s_lshl_b32 s6, s36, 12
	v_lshrrev_b32_e32 v2, 29, v2
	s_add_u32 s0, s0, s6
	v_add_u32_e32 v2, v22, v2
	s_addc_u32 s1, s1, 0
	v_ashrrev_i32_e32 v128, 3, v2
	v_and_b32_e32 v2, -8, v2
	s_add_u32 s6, s0, 0xca00000
	v_sub_u32_e32 v24, v22, v2
	v_lshlrev_b32_e32 v2, 4, v22
	s_addc_u32 s7, s1, 0
	v_ashrrev_i32_e32 v23, 3, v22
	v_and_b32_e32 v130, 0x70, v2
	v_mov_b32_e32 v131, v3
	v_lshl_add_u64 v[132:133], s[6:7], 0, v[130:131]
	v_add_u32_e32 v25, 64, v23
	v_mad_i64_i32 v[8:9], s[0:1], v23, s55, v[132:133]
	v_mad_i64_i32 v[12:13], s[0:1], v25, s55, v[132:133]
	v_readfirstlane_b32 s0, v22
	s_ashr_i32 s12, s0, 1
	v_ashrrev_i32_e32 v129, 31, v128
	v_lshlrev_b32_e32 v6, 3, v24
	v_mov_b32_e32 v2, s12
	s_movk_i32 s0, 0xffe0
	v_lshlrev_b64 v[4:5], 10, v[128:129]
	v_ashrrev_i32_e32 v7, 31, v6
	v_bfi_b32 v20, s0, v2, v22
	v_lshl_add_u64 v[4:5], s[26:27], 0, v[4:5]
	v_lshlrev_b64 v[16:17], 1, v[6:7]
	v_ashrrev_i32_e32 v21, 31, v20
	v_lshl_add_u64 v[18:19], v[4:5], 0, v[16:17]
	v_bfe_u32 v26, v22, 5, 1
	v_lshlrev_b64 v[20:21], 10, v[20:21]
	s_mov_b32 s0, 0x10000
	global_load_dwordx4 v[4:7], v[18:19], off
	s_nop 0
	global_load_dwordx4 v[8:11], v[8:9], off
	v_lshl_add_u64 v[20:21], s[24:25], 0, v[20:21]
	v_lshlrev_b32_e32 v2, 4, v26
	v_add_co_u32_e32 v18, vcc, s0, v18
	v_lshl_add_u64 v[20:21], v[20:21], 0, v[2:3]
	s_nop 0
	v_addc_co_u32_e32 v19, vcc, 0, v19, vcc
	global_load_dwordx4 v[12:15], v[12:13], off
	s_nop 0
	global_load_dwordx4 v[112:115], v[20:21], off
	global_load_dwordx4 v[108:111], v[20:21], off offset:32
	global_load_dwordx4 v[104:107], v[20:21], off offset:64
	global_load_dwordx4 v[100:103], v[20:21], off offset:96
	global_load_dwordx4 v[116:119], v[18:19], off
	v_mov_b64_e32 v[18:19], s[6:7]
	v_mad_i64_i32 v[20:21], s[0:1], v23, s55, v[18:19]
	v_lshl_add_u64 v[20:21], v[20:21], 0, v[130:131]
	v_mad_i64_i32 v[18:19], s[0:1], v25, s55, v[18:19]
	v_lshl_add_u64 v[18:19], v[18:19], 0, v[130:131]
	global_load_dwordx4 v[120:123], v[20:21], off offset:128
	global_load_dwordx4 v[124:127], v[18:19], off offset:128
	v_lshlrev_b32_e32 v18, 1, v22
	v_lshrrev_b32_e32 v19, 1, v22
	s_movk_i32 s33, 0x90
	v_and_b32_e32 v18, 8, v18
	v_and_b32_e32 v19, 4, v19
	v_and_b32_e32 v20, 19, v22
	v_mul_lo_u32 v144, v128, s33
	v_lshlrev_b32_e32 v146, 4, v24
	v_or3_b32 v18, v18, v20, v19
	v_add3_u32 v19, 0, v144, v146
	v_mul_lo_u32 v147, v23, s33
	v_and_b32_e32 v142, 31, v22
	s_andn2_b32 s12, s12, 31
	v_mul_i32_i24_e32 v143, -8, v26
	s_lshl_b32 s35, s92, 8
	v_mul_u32_u24_e32 v148, 0x90, v18
	v_mov_b32_e32 v18, v3
	s_add_i32 s0, s12, s48
	v_mad_i64_i32 v[134:135], s[50:51], v23, s55, 0
	v_mad_i64_i32 v[136:137], s[50:51], v25, s55, 0
	v_lshl_add_u64 v[138:139], s[26:27], 0, v[16:17]
	v_mov_b32_e32 v16, v3
	v_mov_b32_e32 v17, v3
	v_readfirstlane_b32 s1, v145
	s_mov_b32 s31, 1
	s_or_b32 s13, s0, 31
	v_mul_u32_u24_e32 v129, 0x90, v142
	v_mov_b32_e32 v131, 0xf149f2ca
	v_mov_b32_e32 v141, 0
	s_movk_i32 s84, 0x80
	s_waitcnt vmcnt(0)
	ds_write_b128 v19, v[4:7]
	s_mov_b32 s64, 0xb400
	v_readfirstlane_b32 s99, v0
	s_lshr_b32 s99, s99, 8
	v_add3_u32 v4, s64, v130, v147
	ds_write_b128 v4, v[8:11] offset:9216
	ds_write_b128 v4, v[12:15] offset:18432
	v_add3_u32 v4, v143, s12, v142
	v_subrev_u32_e32 v4, s35, v4
	v_mov_b32_e32 v19, v3
	v_add_u32_e32 v149, 0x6e9, v4
	v_mov_b32_e32 v4, v3
	v_mov_b32_e32 v5, v3
	v_mov_b32_e32 v6, v3
	v_mov_b32_e32 v7, v3
	v_mov_b32_e32 v8, v3
	v_mov_b32_e32 v9, v3
	v_mov_b32_e32 v10, v3
	v_mov_b32_e32 v11, v3
	v_mov_b32_e32 v12, v3
	v_mov_b32_e32 v13, v3
	v_mov_b32_e32 v14, v3
	v_mov_b32_e32 v15, v3
	v_mov_b64_e32 v[34:35], v[18:19]
	v_mov_b64_e32 v[50:51], v[18:19]
	v_mov_b64_e32 v[66:67], v[18:19]
	v_mov_b64_e32 v[32:33], v[16:17]
	v_mov_b64_e32 v[30:31], v[14:15]
	v_mov_b64_e32 v[28:29], v[12:13]
	v_mov_b64_e32 v[26:27], v[10:11]
	v_mov_b64_e32 v[24:25], v[8:9]
	v_mov_b64_e32 v[22:23], v[6:7]
	v_mov_b64_e32 v[20:21], v[4:5]
	v_mov_b64_e32 v[48:49], v[16:17]
	v_mov_b64_e32 v[46:47], v[14:15]
	v_mov_b64_e32 v[44:45], v[12:13]
	v_mov_b64_e32 v[42:43], v[10:11]
	v_mov_b64_e32 v[40:41], v[8:9]
	v_mov_b64_e32 v[38:39], v[6:7]
	v_mov_b64_e32 v[36:37], v[4:5]
	v_mov_b64_e32 v[64:65], v[16:17]
	v_mov_b64_e32 v[62:63], v[14:15]
	v_mov_b64_e32 v[60:61], v[12:13]
	v_mov_b64_e32 v[58:59], v[10:11]
	v_mov_b64_e32 v[56:57], v[8:9]
	v_mov_b64_e32 v[54:55], v[6:7]
	v_mov_b64_e32 v[52:53], v[4:5]
	s_waitcnt lgkmcnt(0)
	s_barrier
.LBB6_1254:
	s_add_i32 s65, s64, 0x4800
	s_cmp_eq_u32 s65, 0x18c00
	s_cselect_b32 s65, 0xb400, s65
	s_and_b32 s45, 1, s31
	s_cselect_b32 s12, 0x6c00, 0
	s_add_i32 s12, s12, 0
	v_add3_u32 v68, s12, v144, v146
	s_add_i32 s33, s31, 1
	s_waitcnt vmcnt(2)
	ds_write_b128 v68, v[116:119]
	v_add3_u32 v68, s65, v130, v147
	s_cmp_ge_u32 s33, s47
	s_waitcnt vmcnt(1)
	ds_write_b128 v68, v[120:123] offset:9216
	s_waitcnt vmcnt(0)
	ds_write_b128 v68, v[124:127] offset:18432
	s_cbranch_scc1 .LBB6_1256
	v_add_u32_e32 v68, s84, v128
	v_ashrrev_i32_e32 v69, 31, v68
	v_lshlrev_b64 v[68:69], 10, v[68:69]
	v_lshl_add_u64 v[68:69], v[138:139], 0, v[68:69]
	v_lshl_add_u64 v[70:71], s[84:85], 1, v[132:133]
	v_lshl_add_u64 v[72:73], v[70:71], 0, v[134:135]
	global_load_dwordx4 v[116:119], v[68:69], off
	global_load_dwordx4 v[120:123], v[72:73], off
	v_lshl_add_u64 v[68:69], v[70:71], 0, v[136:137]
	global_load_dwordx4 v[124:127], v[68:69], off

.LBB6_1261:
	v_cndmask_b32_e32 v131, v150, v131, vcc
	v_sub_f32_e32 v99, v99, v131
	v_sub_f32_e32 v98, v98, v131
	v_sub_f32_e32 v97, v97, v131
	v_sub_f32_e32 v96, v96, v131
	v_sub_f32_e32 v95, v95, v131
	v_sub_f32_e32 v94, v94, v131
	v_sub_f32_e32 v93, v93, v131
	v_sub_f32_e32 v92, v92, v131
	v_sub_f32_e32 v91, v91, v131
	v_sub_f32_e32 v90, v90, v131
	v_sub_f32_e32 v89, v89, v131
	v_sub_f32_e32 v88, v88, v131
	v_sub_f32_e32 v87, v87, v131
	v_sub_f32_e32 v86, v86, v131
	v_sub_f32_e32 v85, v85, v131
	v_sub_f32_e32 v84, v84, v131
	v_sub_f32_e32 v150, v83, v131
	v_sub_f32_e32 v151, v82, v131
	v_sub_f32_e32 v152, v81, v131
	v_sub_f32_e32 v153, v80, v131
	v_sub_f32_e32 v154, v79, v131
	v_sub_f32_e32 v155, v78, v131
	v_sub_f32_e32 v156, v77, v131
	v_sub_f32_e32 v157, v76, v131
	v_sub_f32_e32 v83, v75, v131
	v_sub_f32_e32 v75, v74, v131
	v_sub_f32_e32 v74, v73, v131
	v_sub_f32_e32 v73, v72, v131
	v_sub_f32_e32 v72, v71, v131
	v_sub_f32_e32 v71, v70, v131
	v_sub_f32_e32 v70, v69, v131
	v_sub_f32_e32 v69, v68, v131
	v_exp_f32_e32 v68, v84
	v_exp_f32_e32 v76, v69
	v_exp_f32_e32 v69, v85
	v_exp_f32_e32 v77, v70
	v_exp_f32_e32 v70, v86
	v_exp_f32_e32 v78, v71
	v_exp_f32_e32 v71, v87
	v_exp_f32_e32 v79, v72
	v_exp_f32_e32 v72, v88
	v_exp_f32_e32 v80, v73
	v_exp_f32_e32 v73, v89
	v_exp_f32_e32 v81, v74
	v_exp_f32_e32 v74, v90
	v_exp_f32_e32 v82, v75
	v_exp_f32_e32 v75, v91
	v_exp_f32_e32 v83, v83
	v_exp_f32_e32 v84, v92
	v_exp_f32_e32 v86, v157
	v_exp_f32_e32 v85, v93
	v_exp_f32_e32 v87, v156
	v_exp_f32_e32 v88, v94
	v_exp_f32_e32 v90, v155
	v_exp_f32_e32 v89, v95
	v_exp_f32_e32 v91, v154
	v_exp_f32_e32 v92, v96
	v_exp_f32_e32 v94, v153
	v_exp_f32_e32 v93, v97
	v_exp_f32_e32 v95, v152
	v_exp_f32_e32 v96, v98
	v_exp_f32_e32 v98, v151
	v_exp_f32_e32 v97, v99
	v_exp_f32_e32 v99, v150
	v_pk_add_f32 v[150:151], v[90:91], v[88:89]
	v_pk_add_f32 v[152:153], v[78:79], v[70:71]
	v_pk_add_f32 v[156:157], v[82:83], v[74:75]
	v_pk_add_f32 v[154:155], v[98:99], v[96:97]
	v_pk_add_f32 v[158:159], v[86:87], v[84:85]
	v_pk_add_f32 v[160:161], v[76:77], v[68:69]
	v_pk_add_f32 v[162:163], v[94:95], v[92:93]
	v_pk_add_f32 v[164:165], v[80:81], v[72:73]
	v_pk_add_f32 v[158:159], v[160:161], v[158:159]
	v_pk_add_f32 v[162:163], v[164:165], v[162:163]
	v_pk_add_f32 v[154:155], v[156:157], v[154:155]
	v_pk_add_f32 v[150:151], v[152:153], v[150:151]
	v_pk_add_f32 v[152:153], v[158:159], v[162:163]
	v_pk_add_f32 v[150:151], v[150:151], v[154:155]
	v_cndmask_b32_e64 v140, v140, 1.0, vcc
	v_pk_add_f32 v[150:151], v[152:153], v[150:151]
	v_cvt_pk_bf16_f32 v68, v68, v69
	v_add_f32_e32 v166, v150, v151
	v_fmac_f32_e32 v166, v141, v140
	v_cvt_pk_bf16_f32 v69, v70, v71
	v_cvt_pk_bf16_f32 v71, v74, v75
	v_cvt_pk_bf16_f32 v75, v96, v97
	v_add3_u32 v96, s64, v129, v2
	v_add3_u32 v140, s64, v2, v129
	v_cvt_pk_bf16_f32 v70, v72, v73
	v_cvt_pk_bf16_f32 v72, v84, v85
	v_cvt_pk_bf16_f32 v73, v88, v89
	v_cvt_pk_bf16_f32 v74, v92, v93
	v_cvt_pk_bf16_f32 v76, v76, v77
	v_cvt_pk_bf16_f32 v77, v78, v79
	v_cvt_pk_bf16_f32 v78, v80, v81
	v_cvt_pk_bf16_f32 v79, v82, v83
	v_cvt_pk_bf16_f32 v80, v86, v87
	v_cvt_pk_bf16_f32 v81, v90, v91
	v_cvt_pk_bf16_f32 v82, v94, v95
	v_cvt_pk_bf16_f32 v83, v98, v99
	s_cmp_eq_u32 s99, 0
	s_cbranch_scc1 .Latt_nomid_a1
	s_waitcnt lgkmcnt(0)
	s_barrier
.Latt_nomid_a1:
	ds_read_b128 v[84:87], v96 offset:9216
	ds_read_b128 v[88:91], v96 offset:9248
	ds_read_b128 v[92:95], v96 offset:9280
	ds_read_b128 v[96:99], v96 offset:9312
	ds_read_b128 v[150:153], v140 offset:13824
	ds_read_b128 v[154:157], v140 offset:13856
	ds_read_b128 v[158:161], v140 offset:13888
	ds_read_b128 v[162:165], v140 offset:13920
	s_waitcnt lgkmcnt(7)
	v_mfma_f32_32x32x16_bf16 v[52:67], v[84:87], v[68:71], v[52:67]
	s_waitcnt lgkmcnt(6)
	v_mfma_f32_32x32x16_bf16 v[52:67], v[88:91], v[72:75], v[52:67]
	s_waitcnt lgkmcnt(5)
	v_mfma_f32_32x32x16_bf16 v[52:67], v[92:95], v[76:79], v[52:67]
	s_waitcnt lgkmcnt(4)
	v_mfma_f32_32x32x16_bf16 v[52:67], v[96:99], v[80:83], v[52:67]
	ds_read_b128 v[84:87], v140 offset:18432
	ds_read_b128 v[88:91], v140 offset:18464
	ds_read_b128 v[92:95], v140 offset:18496
	ds_read_b128 v[96:99], v140 offset:18528
	s_waitcnt lgkmcnt(7)
	v_mfma_f32_32x32x16_bf16 v[36:51], v[150:153], v[68:71], v[36:51]
	s_waitcnt lgkmcnt(6)
	v_mfma_f32_32x32x16_bf16 v[36:51], v[154:157], v[72:75], v[36:51]
	s_waitcnt lgkmcnt(5)
	v_mfma_f32_32x32x16_bf16 v[36:51], v[158:161], v[76:79], v[36:51]
	s_waitcnt lgkmcnt(4)
	v_mfma_f32_32x32x16_bf16 v[36:51], v[162:165], v[80:83], v[36:51]
	ds_read_b128 v[150:153], v140 offset:23040
	ds_read_b128 v[154:157], v140 offset:23072
	ds_read_b128 v[158:161], v140 offset:23104
	ds_read_b128 v[162:165], v140 offset:23136
	s_waitcnt lgkmcnt(7)
	v_mfma_f32_32x32x16_bf16 v[20:35], v[84:87], v[68:71], v[20:35]
	s_waitcnt lgkmcnt(6)
	v_mfma_f32_32x32x16_bf16 v[20:35], v[88:91], v[72:75], v[20:35]
	s_waitcnt lgkmcnt(5)
	v_mfma_f32_32x32x16_bf16 v[20:35], v[92:95], v[76:79], v[20:35]
	s_waitcnt lgkmcnt(4)
	v_mfma_f32_32x32x16_bf16 v[20:35], v[96:99], v[80:83], v[20:35]
	s_waitcnt lgkmcnt(3)
	v_mfma_f32_32x32x16_bf16 v[4:19], v[150:153], v[68:71], v[4:19]
	s_waitcnt lgkmcnt(2)
	v_mfma_f32_32x32x16_bf16 v[4:19], v[154:157], v[72:75], v[4:19]
	s_waitcnt lgkmcnt(1)
	v_mfma_f32_32x32x16_bf16 v[4:19], v[158:161], v[76:79], v[4:19]
	s_waitcnt lgkmcnt(0)
	v_mfma_f32_32x32x16_bf16 v[4:19], v[162:165], v[80:83], v[4:19]
	v_mov_b32_e32 v141, v166
.LBB6_1262:
	s_add_i32 s84, s84, 64
	v_subrev_u32_e32 v149, 64, v149
	s_mov_b32 s64, s65
	s_waitcnt lgkmcnt(0)
	s_cmp_lg_u32 s99, 0
	s_cbranch_scc1 .Latt_nobot_a1
	s_barrier
.Latt_nobot_a1:
	s_cmp_lg_u32 s47, s33
	s_cbranch_scc0 .LBB6_1264
	s_mov_b32 s31, s33
	s_branch .LBB6_1254
.Latt_skip_a1:
	s_cmp_eq_u32 s99, 0
	s_cbranch_scc1 .LBB6_1262
	s_waitcnt lgkmcnt(0)
	s_barrier
	s_branch .LBB6_1262

.LBB6_1269:
	v_cndmask_b32_e32 v101, v101, v131, vcc
	v_cndmask_b32_e64 v116, v100, 1.0, vcc
	v_sub_f32_e32 v99, v99, v101
	v_sub_f32_e32 v98, v98, v101
	v_sub_f32_e32 v97, v97, v101
	v_sub_f32_e32 v96, v96, v101
	v_sub_f32_e32 v95, v95, v101
	v_sub_f32_e32 v94, v94, v101
	v_sub_f32_e32 v93, v93, v101
	v_sub_f32_e32 v92, v92, v101
	v_sub_f32_e32 v91, v91, v101
	v_sub_f32_e32 v90, v90, v101
	v_sub_f32_e32 v89, v89, v101
	v_sub_f32_e32 v88, v88, v101
	v_sub_f32_e32 v87, v87, v101
	v_sub_f32_e32 v86, v86, v101
	v_sub_f32_e32 v85, v85, v101
	v_sub_f32_e32 v84, v84, v101
	v_sub_f32_e32 v100, v83, v101
	v_sub_f32_e32 v102, v82, v101
	v_sub_f32_e32 v103, v81, v101
	v_sub_f32_e32 v104, v80, v101
	v_sub_f32_e32 v105, v79, v101
	v_sub_f32_e32 v106, v78, v101
	v_sub_f32_e32 v107, v77, v101
	v_sub_f32_e32 v108, v76, v101
	v_sub_f32_e32 v83, v75, v101
	v_sub_f32_e32 v75, v74, v101
	v_sub_f32_e32 v74, v73, v101
	v_sub_f32_e32 v73, v72, v101
	v_sub_f32_e32 v72, v71, v101
	v_sub_f32_e32 v71, v70, v101
	v_sub_f32_e32 v70, v69, v101
	v_sub_f32_e32 v69, v68, v101
	v_exp_f32_e32 v68, v84
	v_exp_f32_e32 v76, v69
	v_exp_f32_e32 v69, v85
	v_exp_f32_e32 v77, v70
	v_exp_f32_e32 v70, v86
	v_exp_f32_e32 v78, v71
	v_exp_f32_e32 v71, v87
	v_exp_f32_e32 v79, v72
	v_exp_f32_e32 v72, v88
	v_exp_f32_e32 v80, v73
	v_exp_f32_e32 v73, v89
	v_exp_f32_e32 v81, v74
	v_exp_f32_e32 v74, v90
	v_exp_f32_e32 v82, v75
	v_exp_f32_e32 v75, v91
	v_exp_f32_e32 v83, v83
	v_exp_f32_e32 v84, v92
	v_exp_f32_e32 v86, v108
	v_exp_f32_e32 v85, v93
	v_exp_f32_e32 v87, v107
	v_exp_f32_e32 v88, v94
	v_exp_f32_e32 v90, v106
	v_exp_f32_e32 v89, v95
	v_exp_f32_e32 v91, v105
	v_exp_f32_e32 v92, v96
	v_exp_f32_e32 v94, v104
	v_exp_f32_e32 v93, v97
	v_exp_f32_e32 v95, v103
	v_exp_f32_e32 v96, v98
	v_exp_f32_e32 v98, v102
	v_exp_f32_e32 v97, v99
	v_exp_f32_e32 v99, v100
	v_pk_add_f32 v[100:101], v[90:91], v[88:89]
	v_pk_add_f32 v[102:103], v[78:79], v[70:71]
	v_pk_add_f32 v[106:107], v[82:83], v[74:75]
	v_pk_add_f32 v[104:105], v[98:99], v[96:97]
	v_pk_add_f32 v[108:109], v[86:87], v[84:85]
	v_pk_add_f32 v[110:111], v[76:77], v[68:69]
	v_pk_add_f32 v[112:113], v[94:95], v[92:93]
	v_pk_add_f32 v[114:115], v[80:81], v[72:73]
	v_pk_add_f32 v[108:109], v[110:111], v[108:109]
	v_pk_add_f32 v[112:113], v[114:115], v[112:113]
	v_pk_add_f32 v[104:105], v[106:107], v[104:105]
	v_pk_add_f32 v[100:101], v[102:103], v[100:101]
	v_pk_add_f32 v[102:103], v[108:109], v[112:113]
	v_pk_add_f32 v[100:101], v[100:101], v[104:105]
	v_cvt_pk_bf16_f32 v68, v68, v69
	v_pk_add_f32 v[100:101], v[102:103], v[100:101]
	v_cvt_pk_bf16_f32 v69, v70, v71
	v_cvt_pk_bf16_f32 v71, v74, v75
	v_cvt_pk_bf16_f32 v75, v96, v97
	v_add3_u32 v96, s64, v129, v2
	v_add3_u32 v2, s64, v2, v129
	v_add_f32_e32 v117, v100, v101
	v_cvt_pk_bf16_f32 v70, v72, v73
	v_cvt_pk_bf16_f32 v72, v84, v85
	v_cvt_pk_bf16_f32 v73, v88, v89
	v_cvt_pk_bf16_f32 v74, v92, v93
	v_cvt_pk_bf16_f32 v76, v76, v77
	v_cvt_pk_bf16_f32 v77, v78, v79
	v_cvt_pk_bf16_f32 v78, v80, v81
	v_cvt_pk_bf16_f32 v79, v82, v83
	v_cvt_pk_bf16_f32 v80, v86, v87
	v_cvt_pk_bf16_f32 v81, v90, v91
	v_cvt_pk_bf16_f32 v82, v94, v95
	v_cvt_pk_bf16_f32 v83, v98, v99
	ds_read_b128 v[84:87], v96 offset:9216
	ds_read_b128 v[88:91], v96 offset:9248
	ds_read_b128 v[92:95], v96 offset:9280
	ds_read_b128 v[96:99], v96 offset:9312
	ds_read_b128 v[100:103], v2 offset:13824
	ds_read_b128 v[104:107], v2 offset:13856
	ds_read_b128 v[108:111], v2 offset:13888
	ds_read_b128 v[112:115], v2 offset:13920
	v_fmac_f32_e32 v117, v141, v116
	s_waitcnt lgkmcnt(7)
	v_mfma_f32_32x32x16_bf16 v[52:67], v[84:87], v[68:71], v[52:67]
	s_waitcnt lgkmcnt(6)
	v_mfma_f32_32x32x16_bf16 v[52:67], v[88:91], v[72:75], v[52:67]
	s_waitcnt lgkmcnt(5)
	v_mfma_f32_32x32x16_bf16 v[52:67], v[92:95], v[76:79], v[52:67]
	s_waitcnt lgkmcnt(4)
	v_mfma_f32_32x32x16_bf16 v[52:67], v[96:99], v[80:83], v[52:67]
	ds_read_b128 v[84:87], v2 offset:18432
	ds_read_b128 v[88:91], v2 offset:18464
	ds_read_b128 v[92:95], v2 offset:18496
	ds_read_b128 v[96:99], v2 offset:18528
	s_waitcnt lgkmcnt(7)
	v_mfma_f32_32x32x16_bf16 v[36:51], v[100:103], v[68:71], v[36:51]
	s_waitcnt lgkmcnt(6)
	v_mfma_f32_32x32x16_bf16 v[36:51], v[104:107], v[72:75], v[36:51]
	s_waitcnt lgkmcnt(5)
	v_mfma_f32_32x32x16_bf16 v[36:51], v[108:111], v[76:79], v[36:51]
	s_waitcnt lgkmcnt(4)
	v_mfma_f32_32x32x16_bf16 v[36:51], v[112:115], v[80:83], v[36:51]
	ds_read_b128 v[100:103], v2 offset:23040
	ds_read_b128 v[104:107], v2 offset:23072
	ds_read_b128 v[108:111], v2 offset:23104
	ds_read_b128 v[112:115], v2 offset:23136
	s_waitcnt lgkmcnt(7)
	v_mfma_f32_32x32x16_bf16 v[20:35], v[84:87], v[68:71], v[20:35]
	s_waitcnt lgkmcnt(6)
	v_mfma_f32_32x32x16_bf16 v[20:35], v[88:91], v[72:75], v[20:35]
	s_waitcnt lgkmcnt(5)
	v_mfma_f32_32x32x16_bf16 v[20:35], v[92:95], v[76:79], v[20:35]
	s_waitcnt lgkmcnt(4)
	v_mfma_f32_32x32x16_bf16 v[20:35], v[96:99], v[80:83], v[20:35]
	s_waitcnt lgkmcnt(3)
	v_mfma_f32_32x32x16_bf16 v[4:19], v[100:103], v[68:71], v[4:19]
	s_waitcnt lgkmcnt(2)
	v_mfma_f32_32x32x16_bf16 v[4:19], v[104:107], v[72:75], v[4:19]
	s_waitcnt lgkmcnt(1)
	v_mfma_f32_32x32x16_bf16 v[4:19], v[108:111], v[76:79], v[4:19]
	s_waitcnt lgkmcnt(0)
	v_mfma_f32_32x32x16_bf16 v[4:19], v[112:115], v[80:83], v[4:19]
	v_mov_b32_e32 v141, v117
.LBB6_1270:
	v_xor_b32_e32 v2, 32, v213
	v_add_u32_e32 v146, 64, v214
	v_cmp_lt_i32_e32 vcc, v2, v146
	s_ashr_i32 s0, s1, 1
	s_andn2_b32 s0, s0, 31
	v_cndmask_b32_e32 v2, v213, v2, vcc
	v_lshlrev_b32_e32 v131, 2, v2
	ds_bpermute_b32 v2, v131, v141
	s_add_i32 s0, s0, s34
	v_and_or_b32 v68, v145, 31, s0
	v_ashrrev_i32_e32 v69, 31, v68
	v_lshlrev_b64 v[68:69], 10, v[68:69]
	s_waitcnt lgkmcnt(0)
	v_add_f32_e32 v2, v141, v2
	v_div_scale_f32 v70, s[0:1], v2, v2, 1.0
	v_rcp_f32_e32 v71, v70
	v_lshl_add_u64 v[68:69], s[28:29], 0, v[68:69]
	s_mov_b32 s31, s85
	v_lshl_add_u64 v[68:69], v[68:69], 0, s[30:31]
	v_fma_f32 v72, -v70, v71, 1.0
	v_fmac_f32_e32 v71, v72, v71
	v_div_scale_f32 v72, vcc, 1.0, v2, 1.0
	v_mul_f32_e32 v73, v72, v71
	v_fma_f32 v74, -v70, v73, v72
	v_fmac_f32_e32 v73, v74, v71
	v_fma_f32 v70, -v70, v73, v72
	v_div_fmas_f32 v70, v70, v71, v73
	v_div_fixup_f32 v70, v70, v2, 1.0
	v_lshrrev_b32_e32 v2, 3, v145
	v_and_b32_e32 v130, 4, v2
	v_lshlrev_b32_e32 v2, 1, v130
	v_lshl_add_u64 v[68:69], v[68:69], 0, v[2:3]
	s_mov_b64 s[0:1], 0x18c00000
	v_lshl_add_u64 v[128:129], v[68:69], 0, s[0:1]
	v_pk_mul_f32 v[52:53], v[52:53], v[70:71] op_sel_hi:[1,0]
	v_pk_mul_f32 v[54:55], v[54:55], v[70:71] op_sel_hi:[1,0]
	s_mov_b32 s0, 0x18c00000
	v_cvt_pk_bf16_f32 v52, v52, v53
	v_cvt_pk_bf16_f32 v53, v54, v55
	v_add_co_u32_e32 v54, vcc, s0, v68
	v_pk_mul_f32 v[36:37], v[36:37], v[70:71] op_sel_hi:[1,0]
	v_pk_mul_f32 v[38:39], v[38:39], v[70:71] op_sel_hi:[1,0]
	v_pk_mul_f32 v[20:21], v[20:21], v[70:71] op_sel_hi:[1,0]
	v_pk_mul_f32 v[22:23], v[22:23], v[70:71] op_sel_hi:[1,0]
	v_pk_mul_f32 v[4:5], v[4:5], v[70:71] op_sel_hi:[1,0]
	v_pk_mul_f32 v[6:7], v[6:7], v[70:71] op_sel_hi:[1,0]
	v_addc_co_u32_e32 v55, vcc, 0, v69, vcc
	v_cvt_pk_bf16_f32 v36, v36, v37
	v_cvt_pk_bf16_f32 v37, v38, v39
	v_cvt_pk_bf16_f32 v20, v20, v21
	v_cvt_pk_bf16_f32 v21, v22, v23
	v_cvt_pk_bf16_f32 v4, v4, v5
	v_cvt_pk_bf16_f32 v5, v6, v7
	s_barrier
	flat_store_dwordx2 v[54:55], v[52:53]
	v_pk_mul_f32 v[52:53], v[56:57], v[70:71] op_sel_hi:[1,0]
	v_pk_mul_f32 v[54:55], v[58:59], v[70:71] op_sel_hi:[1,0]
	flat_store_dwordx2 v[128:129], v[36:37] offset:64
	v_pk_mul_f32 v[36:37], v[40:41], v[70:71] op_sel_hi:[1,0]
	v_pk_mul_f32 v[38:39], v[42:43], v[70:71] op_sel_hi:[1,0]
	flat_store_dwordx2 v[128:129], v[20:21] offset:128
	v_pk_mul_f32 v[20:21], v[24:25], v[70:71] op_sel_hi:[1,0]
	v_pk_mul_f32 v[22:23], v[26:27], v[70:71] op_sel_hi:[1,0]
	flat_store_dwordx2 v[128:129], v[4:5] offset:192
	v_pk_mul_f32 v[4:5], v[8:9], v[70:71] op_sel_hi:[1,0]
	v_pk_mul_f32 v[6:7], v[10:11], v[70:71] op_sel_hi:[1,0]
	v_cvt_pk_bf16_f32 v52, v52, v53
	v_cvt_pk_bf16_f32 v53, v54, v55
	v_cvt_pk_bf16_f32 v36, v36, v37
	v_cvt_pk_bf16_f32 v37, v38, v39
	v_cvt_pk_bf16_f32 v20, v20, v21
	v_cvt_pk_bf16_f32 v21, v22, v23
	v_cvt_pk_bf16_f32 v4, v4, v5
	v_cvt_pk_bf16_f32 v5, v6, v7
	flat_store_dwordx2 v[128:129], v[52:53] offset:16
	v_pk_mul_f32 v[52:53], v[60:61], v[70:71] op_sel_hi:[1,0]
	v_pk_mul_f32 v[54:55], v[62:63], v[70:71] op_sel_hi:[1,0]
	flat_store_dwordx2 v[128:129], v[36:37] offset:80
	v_pk_mul_f32 v[36:37], v[44:45], v[70:71] op_sel_hi:[1,0]
	v_pk_mul_f32 v[38:39], v[46:47], v[70:71] op_sel_hi:[1,0]
	flat_store_dwordx2 v[128:129], v[20:21] offset:144
	v_pk_mul_f32 v[20:21], v[28:29], v[70:71] op_sel_hi:[1,0]
	v_pk_mul_f32 v[22:23], v[30:31], v[70:71] op_sel_hi:[1,0]
	flat_store_dwordx2 v[128:129], v[4:5] offset:208
	v_pk_mul_f32 v[4:5], v[12:13], v[70:71] op_sel_hi:[1,0]
	v_pk_mul_f32 v[6:7], v[14:15], v[70:71] op_sel_hi:[1,0]
	v_cvt_pk_bf16_f32 v52, v52, v53
	v_cvt_pk_bf16_f32 v53, v54, v55
	v_cvt_pk_bf16_f32 v36, v36, v37
	v_cvt_pk_bf16_f32 v37, v38, v39
	v_cvt_pk_bf16_f32 v20, v20, v21
	v_cvt_pk_bf16_f32 v21, v22, v23
	v_cvt_pk_bf16_f32 v4, v4, v5
	v_cvt_pk_bf16_f32 v5, v6, v7
	flat_store_dwordx2 v[128:129], v[52:53] offset:32
	v_pk_mul_f32 v[52:53], v[64:65], v[70:71] op_sel_hi:[1,0]
	v_pk_mul_f32 v[54:55], v[66:67], v[70:71] op_sel_hi:[1,0]
	flat_store_dwordx2 v[128:129], v[36:37] offset:96
	v_pk_mul_f32 v[36:37], v[48:49], v[70:71] op_sel_hi:[1,0]
	v_pk_mul_f32 v[38:39], v[50:51], v[70:71] op_sel_hi:[1,0]
	flat_store_dwordx2 v[128:129], v[20:21] offset:160
	v_pk_mul_f32 v[20:21], v[32:33], v[70:71] op_sel_hi:[1,0]
	v_pk_mul_f32 v[22:23], v[34:35], v[70:71] op_sel_hi:[1,0]
	flat_store_dwordx2 v[128:129], v[4:5] offset:224
	v_pk_mul_f32 v[4:5], v[16:17], v[70:71] op_sel_hi:[1,0]
	v_pk_mul_f32 v[6:7], v[18:19], v[70:71] op_sel_hi:[1,0]
	v_cvt_pk_bf16_f32 v52, v52, v53
	v_cvt_pk_bf16_f32 v53, v54, v55
	v_cvt_pk_bf16_f32 v36, v36, v37
	v_cvt_pk_bf16_f32 v37, v38, v39
	v_cvt_pk_bf16_f32 v20, v20, v21
	v_cvt_pk_bf16_f32 v21, v22, v23
	v_cvt_pk_bf16_f32 v4, v4, v5
	v_cvt_pk_bf16_f32 v5, v6, v7
	v_mov_b32_e32 v22, v0
	flat_store_dwordx2 v[128:129], v[52:53] offset:48
	flat_store_dwordx2 v[128:129], v[36:37] offset:112
	flat_store_dwordx2 v[128:129], v[20:21] offset:176
	flat_store_dwordx2 v[128:129], v[4:5] offset:240
	v_mov_b32_e32 v135, v3
	v_ashrrev_i32_e32 v2, 31, v22
	v_lshrrev_b32_e32 v2, 29, v2
	v_add_u32_e32 v2, v22, v2
	v_ashrrev_i32_e32 v132, 3, v2
	v_and_b32_e32 v2, -8, v2
	v_sub_u32_e32 v24, v22, v2
	v_lshlrev_b32_e32 v2, 4, v22
	v_ashrrev_i32_e32 v23, 3, v22
	v_and_b32_e32 v134, 0x70, v2
	v_lshl_add_u64 v[136:137], s[6:7], 0, v[134:135]
	v_add_u32_e32 v25, 64, v23
	v_mad_i64_i32 v[8:9], s[0:1], v23, s55, v[136:137]
	v_mad_i64_i32 v[12:13], s[0:1], v25, s55, v[136:137]
	s_add_u32 s26, s26, 0x80
	v_readfirstlane_b32 s0, v22
	s_addc_u32 s27, s27, 0
	s_ashr_i32 s12, s0, 1
	v_ashrrev_i32_e32 v133, 31, v132
	v_lshlrev_b32_e32 v6, 3, v24
	v_mov_b32_e32 v2, s12
	s_movk_i32 s0, 0xffe0
	v_lshlrev_b64 v[4:5], 10, v[132:133]
	v_ashrrev_i32_e32 v7, 31, v6
	v_bfi_b32 v20, s0, v2, v22
	v_lshl_add_u64 v[4:5], s[26:27], 0, v[4:5]
	v_lshlrev_b64 v[16:17], 1, v[6:7]
	v_ashrrev_i32_e32 v21, 31, v20
	v_lshl_add_u64 v[18:19], v[4:5], 0, v[16:17]
	v_bfe_u32 v26, v22, 5, 1
	v_lshlrev_b64 v[20:21], 10, v[20:21]
	s_mov_b32 s0, 0x10000
	global_load_dwordx4 v[4:7], v[18:19], off
	s_nop 0
	global_load_dwordx4 v[8:11], v[8:9], off
	v_lshl_add_u64 v[20:21], s[24:25], 0, v[20:21]
	v_lshlrev_b32_e32 v2, 4, v26
	v_add_co_u32_e32 v18, vcc, s0, v18
	v_lshl_add_u64 v[20:21], v[20:21], 0, v[2:3]
	s_nop 0
	v_addc_co_u32_e32 v19, vcc, 0, v19, vcc
	global_load_dwordx4 v[12:15], v[12:13], off
	s_nop 0
	global_load_dwordx4 v[112:115], v[20:21], off offset:128
	global_load_dwordx4 v[108:111], v[20:21], off offset:160
	global_load_dwordx4 v[104:107], v[20:21], off offset:192
	global_load_dwordx4 v[100:103], v[20:21], off offset:224
	global_load_dwordx4 v[116:119], v[18:19], off
	v_mov_b64_e32 v[18:19], s[6:7]
	v_mad_i64_i32 v[20:21], s[0:1], v23, s55, v[18:19]
	v_lshl_add_u64 v[20:21], v[20:21], 0, v[134:135]
	v_mad_i64_i32 v[18:19], s[0:1], v25, s55, v[18:19]
	v_lshl_add_u64 v[18:19], v[18:19], 0, v[134:135]
	global_load_dwordx4 v[120:123], v[20:21], off offset:128
	global_load_dwordx4 v[124:127], v[18:19], off offset:128
	s_and_b32 s1, s12, 0xffffffe0
	v_mad_i64_i32 v[138:139], s[12:13], v23, s55, 0
	v_mad_i64_i32 v[140:141], s[12:13], v25, s55, 0
	v_lshlrev_b32_e32 v18, 1, v22
	v_lshrrev_b32_e32 v19, 1, v22
	s_movk_i32 s12, 0x90
	v_and_b32_e32 v18, 8, v18
	v_and_b32_e32 v19, 4, v19
	v_and_b32_e32 v20, 19, v22
	v_mul_lo_u32 v149, v132, s12
	v_lshlrev_b32_e32 v150, 4, v24
	v_or3_b32 v18, v18, v20, v19
	v_add3_u32 v19, 0, v149, v150
	v_mul_lo_u32 v151, v23, s12
	v_and_b32_e32 v147, 31, v22
	v_mul_i32_i24_e32 v148, -8, v26
	v_mov_b32_e32 v20, v3
	v_mov_b32_e32 v21, v3
	v_mov_b32_e32 v34, v3
	v_mov_b32_e32 v35, v3
	s_add_i32 s0, s1, s48
	v_lshl_add_u64 v[142:143], s[26:27], 0, v[16:17]
	v_mul_u32_u24_e32 v152, 0x90, v18
	v_mov_b32_e32 v22, v3
	v_mov_b32_e32 v23, v3
	v_mov_b32_e32 v24, v3
	v_mov_b32_e32 v25, v3
	v_mov_b32_e32 v26, v3
	v_mov_b32_e32 v27, v3
	v_mov_b32_e32 v28, v3
	v_mov_b32_e32 v29, v3
	v_mov_b32_e32 v30, v3
	v_mov_b32_e32 v31, v3
	v_mov_b32_e32 v32, v3
	v_mov_b32_e32 v33, v3
	v_mov_b64_e32 v[50:51], v[34:35]
	v_mov_b64_e32 v[66:67], v[34:35]
	s_mov_b32 s7, 1
	s_or_b32 s6, s0, 31
	s_movk_i32 s41, 0x90
	v_mul_u32_u24_e32 v133, 0x90, v147
	v_mov_b32_e32 v135, 0xf149f2ca
	v_mov_b32_e32 v183, 0
	s_movk_i32 s84, 0x80
	v_mov_b64_e32 v[48:49], v[32:33]
	v_mov_b64_e32 v[46:47], v[30:31]
	v_mov_b64_e32 v[44:45], v[28:29]
	v_mov_b64_e32 v[42:43], v[26:27]
	v_mov_b64_e32 v[40:41], v[24:25]
	v_mov_b64_e32 v[38:39], v[22:23]
	v_mov_b64_e32 v[36:37], v[20:21]
	v_mov_b64_e32 v[64:65], v[32:33]
	v_mov_b64_e32 v[62:63], v[30:31]
	v_mov_b64_e32 v[60:61], v[28:29]
	v_mov_b64_e32 v[58:59], v[26:27]
	v_mov_b64_e32 v[56:57], v[24:25]
	v_mov_b64_e32 v[54:55], v[22:23]
	v_mov_b64_e32 v[52:53], v[20:21]
	s_waitcnt vmcnt(0)
	ds_write_b128 v19, v[4:7]
	s_mov_b32 s64, 0xb400
	v_readfirstlane_b32 s99, v0
	s_lshr_b32 s99, s99, 8
	v_add3_u32 v4, s64, v134, v151
	ds_write_b128 v4, v[8:11] offset:9216
	ds_write_b128 v4, v[12:15] offset:18432
	v_add3_u32 v4, v148, s1, v147
	v_subrev_u32_e32 v4, s35, v4
	v_add_u32_e32 v153, 0x6e9, v4
	v_mov_b64_e32 v[4:5], v[20:21]
	v_mov_b64_e32 v[6:7], v[22:23]
	v_mov_b64_e32 v[8:9], v[24:25]
	v_mov_b64_e32 v[10:11], v[26:27]
	v_mov_b64_e32 v[12:13], v[28:29]
	v_mov_b64_e32 v[14:15], v[30:31]
	v_mov_b64_e32 v[16:17], v[32:33]
	v_mov_b64_e32 v[18:19], v[34:35]
	s_waitcnt lgkmcnt(0)
	s_barrier
.LBB6_1271:
	s_add_i32 s65, s64, 0x4800
	s_cmp_eq_u32 s65, 0x18c00
	s_cselect_b32 s65, 0xb400, s65
	s_and_b32 s13, 1, s7
	s_cselect_b32 s1, 0x6c00, 0
	s_add_i32 s1, s1, 0
	v_add3_u32 v68, s1, v149, v150
	s_add_i32 s12, s7, 1
	s_waitcnt vmcnt(2)
	ds_write_b128 v68, v[116:119]
	v_add3_u32 v68, s65, v134, v151
	s_cmp_ge_u32 s12, s47
	s_waitcnt vmcnt(1)
	ds_write_b128 v68, v[120:123] offset:9216
	s_waitcnt vmcnt(0)
	ds_write_b128 v68, v[124:127] offset:18432
	s_cbranch_scc1 .LBB6_1273
	v_add_u32_e32 v68, s84, v132
	v_ashrrev_i32_e32 v69, 31, v68
	v_lshlrev_b64 v[68:69], 10, v[68:69]
	v_lshl_add_u64 v[68:69], v[142:143], 0, v[68:69]
	v_lshl_add_u64 v[70:71], s[84:85], 1, v[136:137]
	v_lshl_add_u64 v[72:73], v[70:71], 0, v[138:139]
	global_load_dwordx4 v[116:119], v[68:69], off
	global_load_dwordx4 v[120:123], v[72:73], off
	v_lshl_add_u64 v[68:69], v[70:71], 0, v[140:141]
	global_load_dwordx4 v[124:127], v[68:69], off

.LBB6_1278:
	v_cndmask_b32_e32 v135, v154, v135, vcc
	v_sub_f32_e32 v99, v99, v135
	v_sub_f32_e32 v98, v98, v135
	v_sub_f32_e32 v97, v97, v135
	v_sub_f32_e32 v96, v96, v135
	v_sub_f32_e32 v95, v95, v135
	v_sub_f32_e32 v94, v94, v135
	v_sub_f32_e32 v93, v93, v135
	v_sub_f32_e32 v92, v92, v135
	v_sub_f32_e32 v91, v91, v135
	v_sub_f32_e32 v90, v90, v135
	v_sub_f32_e32 v89, v89, v135
	v_sub_f32_e32 v88, v88, v135
	v_sub_f32_e32 v87, v87, v135
	v_sub_f32_e32 v86, v86, v135
	v_sub_f32_e32 v85, v85, v135
	v_sub_f32_e32 v84, v84, v135
	v_sub_f32_e32 v154, v83, v135
	v_sub_f32_e32 v155, v82, v135
	v_sub_f32_e32 v156, v81, v135
	v_sub_f32_e32 v157, v80, v135
	v_sub_f32_e32 v158, v79, v135
	v_sub_f32_e32 v159, v78, v135
	v_sub_f32_e32 v160, v77, v135
	v_sub_f32_e32 v161, v76, v135
	v_sub_f32_e32 v83, v75, v135
	v_sub_f32_e32 v75, v74, v135
	v_sub_f32_e32 v74, v73, v135
	v_sub_f32_e32 v73, v72, v135
	v_sub_f32_e32 v72, v71, v135
	v_sub_f32_e32 v71, v70, v135
	v_sub_f32_e32 v70, v69, v135
	v_sub_f32_e32 v69, v68, v135
	v_exp_f32_e32 v68, v84
	v_exp_f32_e32 v76, v69
	v_exp_f32_e32 v69, v85
	v_exp_f32_e32 v77, v70
	v_exp_f32_e32 v70, v86
	v_exp_f32_e32 v78, v71
	v_exp_f32_e32 v71, v87
	v_exp_f32_e32 v79, v72
	v_exp_f32_e32 v72, v88
	v_exp_f32_e32 v80, v73
	v_exp_f32_e32 v73, v89
	v_exp_f32_e32 v81, v74
	v_exp_f32_e32 v74, v90
	v_exp_f32_e32 v82, v75
	v_exp_f32_e32 v75, v91
	v_exp_f32_e32 v83, v83
	v_exp_f32_e32 v84, v92
	v_exp_f32_e32 v86, v161
	v_exp_f32_e32 v85, v93
	v_exp_f32_e32 v87, v160
	v_exp_f32_e32 v88, v94
	v_exp_f32_e32 v90, v159
	v_exp_f32_e32 v89, v95
	v_exp_f32_e32 v91, v158
	v_exp_f32_e32 v92, v96
	v_exp_f32_e32 v94, v157
	v_exp_f32_e32 v93, v97
	v_exp_f32_e32 v95, v156
	v_exp_f32_e32 v96, v98
	v_exp_f32_e32 v98, v155
	v_exp_f32_e32 v97, v99
	v_exp_f32_e32 v99, v154
	v_pk_add_f32 v[154:155], v[90:91], v[88:89]
	v_pk_add_f32 v[156:157], v[78:79], v[70:71]
	v_pk_add_f32 v[160:161], v[82:83], v[74:75]
	v_pk_add_f32 v[158:159], v[98:99], v[96:97]
	v_pk_add_f32 v[162:163], v[86:87], v[84:85]
	v_pk_add_f32 v[164:165], v[76:77], v[68:69]
	v_pk_add_f32 v[166:167], v[94:95], v[92:93]
	v_pk_add_f32 v[168:169], v[80:81], v[72:73]
	v_pk_add_f32 v[162:163], v[164:165], v[162:163]
	v_pk_add_f32 v[166:167], v[168:169], v[166:167]
	v_pk_add_f32 v[158:159], v[160:161], v[158:159]
	v_pk_add_f32 v[154:155], v[156:157], v[154:155]
	v_pk_add_f32 v[156:157], v[162:163], v[166:167]
	v_pk_add_f32 v[154:155], v[154:155], v[158:159]
	v_cndmask_b32_e64 v144, v144, 1.0, vcc
	v_pk_add_f32 v[154:155], v[156:157], v[154:155]
	v_cvt_pk_bf16_f32 v68, v68, v69
	v_add_f32_e32 v170, v154, v155
	v_fmac_f32_e32 v170, v183, v144
	v_cvt_pk_bf16_f32 v69, v70, v71
	v_cvt_pk_bf16_f32 v71, v74, v75
	v_cvt_pk_bf16_f32 v75, v96, v97
	v_add3_u32 v96, s64, v133, v2
	v_add3_u32 v144, s64, v2, v133
	v_cvt_pk_bf16_f32 v70, v72, v73
	v_cvt_pk_bf16_f32 v72, v84, v85
	v_cvt_pk_bf16_f32 v73, v88, v89
	v_cvt_pk_bf16_f32 v74, v92, v93
	v_cvt_pk_bf16_f32 v76, v76, v77
	v_cvt_pk_bf16_f32 v77, v78, v79
	v_cvt_pk_bf16_f32 v78, v80, v81
	v_cvt_pk_bf16_f32 v79, v82, v83
	v_cvt_pk_bf16_f32 v80, v86, v87
	v_cvt_pk_bf16_f32 v81, v90, v91
	v_cvt_pk_bf16_f32 v82, v94, v95
	v_cvt_pk_bf16_f32 v83, v98, v99
	s_cmp_eq_u32 s99, 0
	s_cbranch_scc1 .Latt_nomid_a2
	s_waitcnt lgkmcnt(0)
	s_barrier
.Latt_nomid_a2:
	ds_read_b128 v[84:87], v96 offset:9216
	ds_read_b128 v[88:91], v96 offset:9248
	ds_read_b128 v[92:95], v96 offset:9280
	ds_read_b128 v[96:99], v96 offset:9312
	ds_read_b128 v[154:157], v144 offset:13824
	ds_read_b128 v[158:161], v144 offset:13856
	ds_read_b128 v[162:165], v144 offset:13888
	ds_read_b128 v[166:169], v144 offset:13920
	s_waitcnt lgkmcnt(7)
	v_mfma_f32_32x32x16_bf16 v[4:19], v[84:87], v[68:71], v[4:19]
	s_waitcnt lgkmcnt(6)
	v_mfma_f32_32x32x16_bf16 v[4:19], v[88:91], v[72:75], v[4:19]
	s_waitcnt lgkmcnt(5)
	v_mfma_f32_32x32x16_bf16 v[4:19], v[92:95], v[76:79], v[4:19]
	s_waitcnt lgkmcnt(4)
	v_mfma_f32_32x32x16_bf16 v[4:19], v[96:99], v[80:83], v[4:19]
	ds_read_b128 v[84:87], v144 offset:18432
	ds_read_b128 v[88:91], v144 offset:18464
	ds_read_b128 v[92:95], v144 offset:18496
	ds_read_b128 v[96:99], v144 offset:18528
	s_waitcnt lgkmcnt(7)
	v_mfma_f32_32x32x16_bf16 v[52:67], v[154:157], v[68:71], v[52:67]
	s_waitcnt lgkmcnt(6)
	v_mfma_f32_32x32x16_bf16 v[52:67], v[158:161], v[72:75], v[52:67]
	s_waitcnt lgkmcnt(5)
	v_mfma_f32_32x32x16_bf16 v[52:67], v[162:165], v[76:79], v[52:67]
	s_waitcnt lgkmcnt(4)
	v_mfma_f32_32x32x16_bf16 v[52:67], v[166:169], v[80:83], v[52:67]
	ds_read_b128 v[154:157], v144 offset:23040
	ds_read_b128 v[158:161], v144 offset:23072
	ds_read_b128 v[162:165], v144 offset:23104
	ds_read_b128 v[166:169], v144 offset:23136
	s_waitcnt lgkmcnt(7)
	v_mfma_f32_32x32x16_bf16 v[36:51], v[84:87], v[68:71], v[36:51]
	s_waitcnt lgkmcnt(6)
	v_mfma_f32_32x32x16_bf16 v[36:51], v[88:91], v[72:75], v[36:51]
	s_waitcnt lgkmcnt(5)
	v_mfma_f32_32x32x16_bf16 v[36:51], v[92:95], v[76:79], v[36:51]
	s_waitcnt lgkmcnt(4)
	v_mfma_f32_32x32x16_bf16 v[36:51], v[96:99], v[80:83], v[36:51]
	s_waitcnt lgkmcnt(3)
	v_mfma_f32_32x32x16_bf16 v[20:35], v[154:157], v[68:71], v[20:35]
	s_waitcnt lgkmcnt(2)
	v_mfma_f32_32x32x16_bf16 v[20:35], v[158:161], v[72:75], v[20:35]
	s_waitcnt lgkmcnt(1)
	v_mfma_f32_32x32x16_bf16 v[20:35], v[162:165], v[76:79], v[20:35]
	s_waitcnt lgkmcnt(0)
	v_mfma_f32_32x32x16_bf16 v[20:35], v[166:169], v[80:83], v[20:35]
	v_mov_b32_e32 v183, v170
.LBB6_1279:
	s_add_i32 s84, s84, 64
	v_subrev_u32_e32 v153, 64, v153
	s_mov_b32 s64, s65
	s_waitcnt lgkmcnt(0)
	s_cmp_lg_u32 s99, 0
	s_cbranch_scc1 .Latt_nobot_a2
	s_barrier
.Latt_nobot_a2:
	s_cmp_lg_u32 s47, s12
	s_cbranch_scc0 .LBB6_1281
	s_mov_b32 s7, s12
	s_branch .LBB6_1271

.LBB6_1286:
	v_cndmask_b32_e32 v101, v101, v135, vcc
	v_cndmask_b32_e64 v116, v100, 1.0, vcc
	v_sub_f32_e32 v99, v99, v101
	v_sub_f32_e32 v98, v98, v101
	v_sub_f32_e32 v97, v97, v101
	v_sub_f32_e32 v96, v96, v101
	v_sub_f32_e32 v95, v95, v101
	v_sub_f32_e32 v94, v94, v101
	v_sub_f32_e32 v93, v93, v101
	v_sub_f32_e32 v92, v92, v101
	v_sub_f32_e32 v91, v91, v101
	v_sub_f32_e32 v90, v90, v101
	v_sub_f32_e32 v89, v89, v101
	v_sub_f32_e32 v88, v88, v101
	v_sub_f32_e32 v87, v87, v101
	v_sub_f32_e32 v86, v86, v101
	v_sub_f32_e32 v85, v85, v101
	v_sub_f32_e32 v84, v84, v101
	v_sub_f32_e32 v100, v83, v101
	v_sub_f32_e32 v102, v82, v101
	v_sub_f32_e32 v103, v81, v101
	v_sub_f32_e32 v104, v80, v101
	v_sub_f32_e32 v105, v79, v101
	v_sub_f32_e32 v106, v78, v101
	v_sub_f32_e32 v107, v77, v101
	v_sub_f32_e32 v108, v76, v101
	v_sub_f32_e32 v83, v75, v101
	v_sub_f32_e32 v75, v74, v101
	v_sub_f32_e32 v74, v73, v101
	v_sub_f32_e32 v73, v72, v101
	v_sub_f32_e32 v72, v71, v101
	v_sub_f32_e32 v71, v70, v101
	v_sub_f32_e32 v70, v69, v101
	v_sub_f32_e32 v69, v68, v101
	v_exp_f32_e32 v68, v84
	v_exp_f32_e32 v76, v69
	v_exp_f32_e32 v69, v85
	v_exp_f32_e32 v77, v70
	v_exp_f32_e32 v70, v86
	v_exp_f32_e32 v78, v71
	v_exp_f32_e32 v71, v87
	v_exp_f32_e32 v79, v72
	v_exp_f32_e32 v72, v88
	v_exp_f32_e32 v80, v73
	v_exp_f32_e32 v73, v89
	v_exp_f32_e32 v81, v74
	v_exp_f32_e32 v74, v90
	v_exp_f32_e32 v82, v75
	v_exp_f32_e32 v75, v91
	v_exp_f32_e32 v83, v83
	v_exp_f32_e32 v84, v92
	v_exp_f32_e32 v86, v108
	v_exp_f32_e32 v85, v93
	v_exp_f32_e32 v87, v107
	v_exp_f32_e32 v88, v94
	v_exp_f32_e32 v90, v106
	v_exp_f32_e32 v89, v95
	v_exp_f32_e32 v91, v105
	v_exp_f32_e32 v92, v96
	v_exp_f32_e32 v94, v104
	v_exp_f32_e32 v93, v97
	v_exp_f32_e32 v95, v103
	v_exp_f32_e32 v96, v98
	v_exp_f32_e32 v98, v102
	v_exp_f32_e32 v97, v99
	v_exp_f32_e32 v99, v100
	v_pk_add_f32 v[100:101], v[90:91], v[88:89]
	v_pk_add_f32 v[102:103], v[78:79], v[70:71]
	v_pk_add_f32 v[106:107], v[82:83], v[74:75]
	v_pk_add_f32 v[104:105], v[98:99], v[96:97]
	v_pk_add_f32 v[108:109], v[86:87], v[84:85]
	v_pk_add_f32 v[110:111], v[76:77], v[68:69]
	v_pk_add_f32 v[112:113], v[94:95], v[92:93]
	v_pk_add_f32 v[114:115], v[80:81], v[72:73]
	v_pk_add_f32 v[108:109], v[110:111], v[108:109]
	v_pk_add_f32 v[112:113], v[114:115], v[112:113]
	v_pk_add_f32 v[104:105], v[106:107], v[104:105]
	v_pk_add_f32 v[100:101], v[102:103], v[100:101]
	v_pk_add_f32 v[102:103], v[108:109], v[112:113]
	v_pk_add_f32 v[100:101], v[100:101], v[104:105]
	v_cvt_pk_bf16_f32 v68, v68, v69
	v_pk_add_f32 v[100:101], v[102:103], v[100:101]
	v_cvt_pk_bf16_f32 v69, v70, v71
	v_cvt_pk_bf16_f32 v71, v74, v75
	v_cvt_pk_bf16_f32 v75, v96, v97
	v_add3_u32 v96, s64, v133, v2
	v_add3_u32 v2, s64, v2, v133
	v_add_f32_e32 v117, v100, v101
	v_cvt_pk_bf16_f32 v70, v72, v73
	v_cvt_pk_bf16_f32 v72, v84, v85
	v_cvt_pk_bf16_f32 v73, v88, v89
	v_cvt_pk_bf16_f32 v74, v92, v93
	v_cvt_pk_bf16_f32 v76, v76, v77
	v_cvt_pk_bf16_f32 v77, v78, v79
	v_cvt_pk_bf16_f32 v78, v80, v81
	v_cvt_pk_bf16_f32 v79, v82, v83
	v_cvt_pk_bf16_f32 v80, v86, v87
	v_cvt_pk_bf16_f32 v81, v90, v91
	v_cvt_pk_bf16_f32 v82, v94, v95
	v_cvt_pk_bf16_f32 v83, v98, v99
	ds_read_b128 v[84:87], v96 offset:9216
	ds_read_b128 v[88:91], v96 offset:9248
	ds_read_b128 v[92:95], v96 offset:9280
	ds_read_b128 v[96:99], v96 offset:9312
	ds_read_b128 v[100:103], v2 offset:13824
	ds_read_b128 v[104:107], v2 offset:13856
	ds_read_b128 v[108:111], v2 offset:13888
	ds_read_b128 v[112:115], v2 offset:13920
	v_fmac_f32_e32 v117, v183, v116
	s_waitcnt lgkmcnt(7)
	v_mfma_f32_32x32x16_bf16 v[4:19], v[84:87], v[68:71], v[4:19]
	s_waitcnt lgkmcnt(6)
	v_mfma_f32_32x32x16_bf16 v[4:19], v[88:91], v[72:75], v[4:19]
	s_waitcnt lgkmcnt(5)
	v_mfma_f32_32x32x16_bf16 v[4:19], v[92:95], v[76:79], v[4:19]
	s_waitcnt lgkmcnt(4)
	v_mfma_f32_32x32x16_bf16 v[4:19], v[96:99], v[80:83], v[4:19]
	ds_read_b128 v[84:87], v2 offset:18432
	ds_read_b128 v[88:91], v2 offset:18464
	ds_read_b128 v[92:95], v2 offset:18496
	ds_read_b128 v[96:99], v2 offset:18528
	s_waitcnt lgkmcnt(7)
	v_mfma_f32_32x32x16_bf16 v[52:67], v[100:103], v[68:71], v[52:67]
	s_waitcnt lgkmcnt(6)
	v_mfma_f32_32x32x16_bf16 v[52:67], v[104:107], v[72:75], v[52:67]
	s_waitcnt lgkmcnt(5)
	v_mfma_f32_32x32x16_bf16 v[52:67], v[108:111], v[76:79], v[52:67]
	s_waitcnt lgkmcnt(4)
	v_mfma_f32_32x32x16_bf16 v[52:67], v[112:115], v[80:83], v[52:67]
	ds_read_b128 v[100:103], v2 offset:23040
	ds_read_b128 v[104:107], v2 offset:23072
	ds_read_b128 v[108:111], v2 offset:23104
	ds_read_b128 v[112:115], v2 offset:23136
	s_waitcnt lgkmcnt(7)
	v_mfma_f32_32x32x16_bf16 v[36:51], v[84:87], v[68:71], v[36:51]
	s_waitcnt lgkmcnt(6)
	v_mfma_f32_32x32x16_bf16 v[36:51], v[88:91], v[72:75], v[36:51]
	s_waitcnt lgkmcnt(5)
	v_mfma_f32_32x32x16_bf16 v[36:51], v[92:95], v[76:79], v[36:51]
	s_waitcnt lgkmcnt(4)
	v_mfma_f32_32x32x16_bf16 v[36:51], v[96:99], v[80:83], v[36:51]
	s_waitcnt lgkmcnt(3)
	v_mfma_f32_32x32x16_bf16 v[20:35], v[100:103], v[68:71], v[20:35]
	s_waitcnt lgkmcnt(2)
	v_mfma_f32_32x32x16_bf16 v[20:35], v[104:107], v[72:75], v[20:35]
	s_waitcnt lgkmcnt(1)
	v_mfma_f32_32x32x16_bf16 v[20:35], v[108:111], v[76:79], v[20:35]
	s_waitcnt lgkmcnt(0)
	v_mfma_f32_32x32x16_bf16 v[20:35], v[112:115], v[80:83], v[20:35]
	v_mov_b32_e32 v183, v117
